# softmax exp stage: packed subtracts + packed partial sums on four accumulators (row sum order changed, same f32 math); on top of v46
# speedup vs baseline: 1.0173x; 1.0050x over previous
.LBB0_1334:
	v_and_b32_e32 v34, 64, v209
	v_xor_b32_e32 v18, 16, v209
	v_add_u32_e32 v19, 64, v34
	v_cmp_lt_i32_e32 vcc, v18, v19
	v_max_f32_e32 v21, v215, v215
	v_mov_b32_e32 v32, v141
	v_cndmask_b32_e32 v18, v209, v18, vcc
	v_lshlrev_b32_e32 v18, 2, v18
	ds_bpermute_b32 v20, v18, v215
	v_mov_b32_e32 v33, v141
	v_readlane_b32 s9, v254, 54
	s_movk_i32 s8, 0x520
	v_lshlrev_b32_e32 v34, 2, v34
	s_waitcnt lgkmcnt(0)
	v_max_f32_e32 v20, v20, v20
	v_max_f32_e32 v20, v21, v20
	v_xor_b32_e32 v21, 32, v209
	v_cmp_lt_i32_e32 vcc, v21, v19
	s_lshl_b64 s[0:1], s[0:1], 9
	s_lshl_b64 s[0:1], s[0:1], 1
	v_cndmask_b32_e32 v19, v209, v21, vcc
	v_lshlrev_b32_e32 v19, 2, v19
	ds_bpermute_b32 v21, v19, v20
	s_waitcnt lgkmcnt(0)
	v_max_f32_e32 v21, v21, v21
	v_max_f32_e32 v20, v20, v21
	v_add_f32_e32 v20, 0xc1000000, v20
	v_pk_add_f32 v[118:119], v[118:119], v[20:21] op_sel_hi:[1,0] neg_lo:[0,1] neg_hi:[0,1]
	v_pk_add_f32 v[120:121], v[120:121], v[20:21] op_sel_hi:[1,0] neg_lo:[0,1] neg_hi:[0,1]
	v_pk_add_f32 v[122:123], v[122:123], v[20:21] op_sel_hi:[1,0] neg_lo:[0,1] neg_hi:[0,1]
	v_pk_add_f32 v[124:125], v[124:125], v[20:21] op_sel_hi:[1,0] neg_lo:[0,1] neg_hi:[0,1]
	v_pk_add_f32 v[126:127], v[126:127], v[20:21] op_sel_hi:[1,0] neg_lo:[0,1] neg_hi:[0,1]
	v_pk_add_f32 v[128:129], v[128:129], v[20:21] op_sel_hi:[1,0] neg_lo:[0,1] neg_hi:[0,1]
	v_pk_add_f32 v[130:131], v[130:131], v[20:21] op_sel_hi:[1,0] neg_lo:[0,1] neg_hi:[0,1]
	v_pk_add_f32 v[132:133], v[132:133], v[20:21] op_sel_hi:[1,0] neg_lo:[0,1] neg_hi:[0,1]
	v_pk_add_f32 v[134:135], v[134:135], v[20:21] op_sel_hi:[1,0] neg_lo:[0,1] neg_hi:[0,1]
	v_pk_add_f32 v[136:137], v[136:137], v[20:21] op_sel_hi:[1,0] neg_lo:[0,1] neg_hi:[0,1]
	v_pk_add_f32 v[156:157], v[156:157], v[20:21] op_sel_hi:[1,0] neg_lo:[0,1] neg_hi:[0,1]
	v_pk_add_f32 v[158:159], v[158:159], v[20:21] op_sel_hi:[1,0] neg_lo:[0,1] neg_hi:[0,1]
	v_pk_add_f32 v[160:161], v[160:161], v[20:21] op_sel_hi:[1,0] neg_lo:[0,1] neg_hi:[0,1]
	v_pk_add_f32 v[162:163], v[162:163], v[20:21] op_sel_hi:[1,0] neg_lo:[0,1] neg_hi:[0,1]
	v_pk_add_f32 v[164:165], v[164:165], v[20:21] op_sel_hi:[1,0] neg_lo:[0,1] neg_hi:[0,1]
	v_pk_add_f32 v[166:167], v[166:167], v[20:21] op_sel_hi:[1,0] neg_lo:[0,1] neg_hi:[0,1]
	v_pk_add_f32 v[168:169], v[168:169], v[20:21] op_sel_hi:[1,0] neg_lo:[0,1] neg_hi:[0,1]
	v_pk_add_f32 v[170:171], v[170:171], v[20:21] op_sel_hi:[1,0] neg_lo:[0,1] neg_hi:[0,1]
	v_pk_add_f32 v[172:173], v[172:173], v[20:21] op_sel_hi:[1,0] neg_lo:[0,1] neg_hi:[0,1]
	v_pk_add_f32 v[174:175], v[174:175], v[20:21] op_sel_hi:[1,0] neg_lo:[0,1] neg_hi:[0,1]
	v_pk_add_f32 v[176:177], v[176:177], v[20:21] op_sel_hi:[1,0] neg_lo:[0,1] neg_hi:[0,1]
	v_pk_add_f32 v[178:179], v[178:179], v[20:21] op_sel_hi:[1,0] neg_lo:[0,1] neg_hi:[0,1]
	v_pk_add_f32 v[180:181], v[180:181], v[20:21] op_sel_hi:[1,0] neg_lo:[0,1] neg_hi:[0,1]
	v_pk_add_f32 v[182:183], v[182:183], v[20:21] op_sel_hi:[1,0] neg_lo:[0,1] neg_hi:[0,1]
	v_pk_add_f32 v[184:185], v[184:185], v[20:21] op_sel_hi:[1,0] neg_lo:[0,1] neg_hi:[0,1]
	v_pk_add_f32 v[186:187], v[186:187], v[20:21] op_sel_hi:[1,0] neg_lo:[0,1] neg_hi:[0,1]
	v_pk_add_f32 v[188:189], v[188:189], v[20:21] op_sel_hi:[1,0] neg_lo:[0,1] neg_hi:[0,1]
	v_pk_add_f32 v[190:191], v[190:191], v[20:21] op_sel_hi:[1,0] neg_lo:[0,1] neg_hi:[0,1]
	v_pk_add_f32 v[192:193], v[192:193], v[20:21] op_sel_hi:[1,0] neg_lo:[0,1] neg_hi:[0,1]
	v_pk_add_f32 v[194:195], v[194:195], v[20:21] op_sel_hi:[1,0] neg_lo:[0,1] neg_hi:[0,1]
	v_pk_add_f32 v[196:197], v[196:197], v[20:21] op_sel_hi:[1,0] neg_lo:[0,1] neg_hi:[0,1]
	v_pk_add_f32 v[198:199], v[198:199], v[20:21] op_sel_hi:[1,0] neg_lo:[0,1] neg_hi:[0,1]
	v_exp_f32_e32 v21, v118
	v_exp_f32_e32 v23, v119
	v_exp_f32_e32 v24, v120
	v_exp_f32_e32 v25, v121
	v_exp_f32_e32 v26, v122
	v_exp_f32_e32 v27, v123
	v_exp_f32_e32 v28, v124
	v_exp_f32_e32 v29, v125
	v_exp_f32_e32 v31, v126
	v_exp_f32_e32 v36, v127
	v_exp_f32_e32 v37, v128
	v_exp_f32_e32 v38, v129
	v_exp_f32_e32 v39, v130
	v_exp_f32_e32 v40, v131
	v_exp_f32_e32 v41, v132
	v_exp_f32_e32 v42, v133
	v_exp_f32_e32 v43, v134
	v_exp_f32_e32 v44, v135
	v_exp_f32_e32 v45, v136
	v_exp_f32_e32 v46, v137
	v_exp_f32_e32 v47, v156
	v_exp_f32_e32 v48, v157
	v_exp_f32_e32 v49, v158
	v_exp_f32_e32 v50, v159
	v_exp_f32_e32 v51, v160
	v_exp_f32_e32 v52, v161
	v_exp_f32_e32 v53, v162
	v_exp_f32_e32 v54, v163
	v_exp_f32_e32 v55, v164
	v_exp_f32_e32 v56, v165
	v_exp_f32_e32 v57, v166
	v_exp_f32_e32 v58, v167
	v_exp_f32_e32 v59, v168
	v_exp_f32_e32 v60, v169
	v_exp_f32_e32 v61, v170
	v_exp_f32_e32 v62, v171
	v_exp_f32_e32 v63, v172
	v_exp_f32_e32 v64, v173
	v_exp_f32_e32 v65, v174
	v_exp_f32_e32 v66, v175
	v_exp_f32_e32 v67, v176
	v_exp_f32_e32 v68, v177
	v_exp_f32_e32 v69, v178
	v_exp_f32_e32 v70, v179
	v_exp_f32_e32 v71, v180
	v_exp_f32_e32 v72, v181
	v_exp_f32_e32 v73, v182
	v_exp_f32_e32 v74, v183
	v_exp_f32_e32 v75, v184
	v_exp_f32_e32 v76, v185
	v_exp_f32_e32 v77, v186
	v_exp_f32_e32 v78, v187
	v_exp_f32_e32 v79, v188
	v_exp_f32_e32 v80, v189
	v_exp_f32_e32 v81, v190
	v_exp_f32_e32 v82, v191
	v_exp_f32_e32 v83, v192
	v_exp_f32_e32 v84, v193
	v_exp_f32_e32 v85, v194
	v_exp_f32_e32 v86, v195
	v_exp_f32_e32 v87, v196
	v_exp_f32_e32 v88, v197
	v_exp_f32_e32 v89, v198
	v_exp_f32_e32 v90, v199
	s_nop 0
	v_pk_add_f32 v[118:119], v[24:25], v[38:39]
	v_pk_add_f32 v[120:121], v[26:27], v[40:41]
	v_pk_add_f32 v[122:123], v[28:29], v[42:43]
	v_pk_add_f32 v[124:125], v[36:37], v[44:45]
	v_pk_add_f32 v[118:119], v[118:119], v[46:47]
	v_pk_add_f32 v[120:121], v[120:121], v[48:49]
	v_pk_add_f32 v[122:123], v[122:123], v[50:51]
	v_pk_add_f32 v[124:125], v[124:125], v[52:53]
	v_pk_add_f32 v[118:119], v[118:119], v[54:55]
	v_pk_add_f32 v[120:121], v[120:121], v[56:57]
	v_pk_add_f32 v[122:123], v[122:123], v[58:59]
	v_pk_add_f32 v[124:125], v[124:125], v[60:61]
	v_pk_add_f32 v[118:119], v[118:119], v[62:63]
	v_pk_add_f32 v[120:121], v[120:121], v[64:65]
	v_pk_add_f32 v[122:123], v[122:123], v[66:67]
	v_pk_add_f32 v[124:125], v[124:125], v[68:69]
	v_pk_add_f32 v[118:119], v[118:119], v[70:71]
	v_pk_add_f32 v[120:121], v[120:121], v[72:73]
	v_pk_add_f32 v[122:123], v[122:123], v[74:75]
	v_pk_add_f32 v[124:125], v[124:125], v[76:77]
	v_pk_add_f32 v[118:119], v[118:119], v[78:79]
	v_pk_add_f32 v[120:121], v[120:121], v[80:81]
	v_pk_add_f32 v[122:123], v[122:123], v[82:83]
	v_pk_add_f32 v[124:125], v[124:125], v[84:85]
	v_pk_add_f32 v[118:119], v[118:119], v[86:87]
	v_pk_add_f32 v[120:121], v[120:121], v[88:89]
	v_pk_add_f32 v[118:119], v[118:119], v[120:121]
	v_pk_add_f32 v[122:123], v[122:123], v[124:125]
	v_add_f32_e32 v126, v21, v23
	v_add_f32_e32 v127, v31, v90
	v_pk_add_f32 v[118:119], v[118:119], v[122:123]
	v_add_f32_e32 v126, v126, v127
	v_add_f32_e32 v20, v118, v119
	v_add_f32_e32 v20, v20, v126
	ds_bpermute_b32 v18, v18, v20
	v_cvt_pk_fp8_f32 v32, v21, v23
	v_cvt_pk_fp8_f32 v33, v26, v27
	v_mov_b32_e32 v30, v141
	v_cvt_pk_fp8_f32 v30, v31, v36
	s_waitcnt lgkmcnt(0)
	v_add_f32_e32 v18, v20, v18
	ds_bpermute_b32 v19, v19, v18
	v_cvt_pk_fp8_f32 v32, v24, v25 op_sel:[0,0,1]
	v_cvt_pk_fp8_f32 v33, v28, v29 op_sel:[0,0,1]
	v_mov_b32_e32 v31, v141
	v_mov_b32_e32 v28, v141
	s_waitcnt lgkmcnt(0)
	v_add_f32_e32 v35, v18, v19
	v_mov_b32_e32 v29, v141
	v_mov_b32_e32 v24, v141
	v_mov_b32_e32 v25, v141
	v_mov_b32_e32 v22, v141
	v_mov_b32_e32 v23, v141
	v_mov_b32_e32 v20, v141
	v_mov_b32_e32 v21, v141
	v_mov_b32_e32 v18, v141
	v_mov_b32_e32 v19, v141
	v_mov_b32_e32 v26, v141
	v_mov_b32_e32 v27, v141
	v_cvt_pk_fp8_f32 v31, v39, v40
	v_cvt_pk_fp8_f32 v28, v43, v44
	v_cvt_pk_fp8_f32 v29, v47, v48
	v_cvt_pk_fp8_f32 v24, v51, v52
	v_cvt_pk_fp8_f32 v25, v55, v56
	v_cvt_pk_fp8_f32 v22, v59, v60
	v_cvt_pk_fp8_f32 v23, v63, v64
	v_cvt_pk_fp8_f32 v20, v67, v68
	v_cvt_pk_fp8_f32 v21, v71, v72
	v_cvt_pk_fp8_f32 v18, v75, v76
	v_cvt_pk_fp8_f32 v19, v79, v80
	v_cvt_pk_fp8_f32 v26, v83, v84
	v_cvt_pk_fp8_f32 v27, v87, v88
	v_cvt_pk_fp8_f32 v30, v37, v38 op_sel:[0,0,1]
	v_cvt_pk_fp8_f32 v31, v41, v42 op_sel:[0,0,1]
	v_cvt_pk_fp8_f32 v28, v45, v46 op_sel:[0,0,1]
	v_cvt_pk_fp8_f32 v29, v49, v50 op_sel:[0,0,1]
	v_cvt_pk_fp8_f32 v24, v53, v54 op_sel:[0,0,1]
	v_cvt_pk_fp8_f32 v25, v57, v58 op_sel:[0,0,1]
	v_cvt_pk_fp8_f32 v22, v61, v62 op_sel:[0,0,1]
	v_cvt_pk_fp8_f32 v23, v65, v66 op_sel:[0,0,1]
	v_cvt_pk_fp8_f32 v20, v69, v70 op_sel:[0,0,1]
	v_cvt_pk_fp8_f32 v21, v73, v74 op_sel:[0,0,1]
	v_cvt_pk_fp8_f32 v18, v77, v78 op_sel:[0,0,1]
	v_cvt_pk_fp8_f32 v19, v81, v82 op_sel:[0,0,1]
	v_cvt_pk_fp8_f32 v26, v85, v86 op_sel:[0,0,1]
	v_cvt_pk_fp8_f32 v27, v89, v90 op_sel:[0,0,1]
	s_nop 0
	ds_read_u16 v86, v212 offset:64
	ds_read_u16 v87, v212 offset:80
	ds_read_u16 v88, v212 offset:96
	ds_read_u16 v89, v212 offset:112
	ds_read_u16 v90, v212 offset:128
	ds_read_u16 v91, v212 offset:144
	ds_read_u16 v92, v212 offset:160
	ds_read_u16 v93, v212 offset:176
	ds_read_u16 v94, v212 offset:192
	ds_read_u16 v95, v212 offset:208
	ds_read_u16 v96, v212 offset:224
	ds_read_u16 v97, v212 offset:240
	ds_read_u16 v98, v212 offset:256
	ds_read_u16 v99, v212 offset:272
	ds_read_u16 v100, v212 offset:288
	ds_read_u16 v101, v212 offset:304
	ds_read_u16 v102, v212 offset:320
	ds_read_u16 v103, v212 offset:336
	ds_read_u16 v104, v212 offset:352
	ds_read_u16 v105, v212 offset:368
	ds_read_u16 v106, v212 offset:384
	ds_read_u16 v107, v212 offset:400
	ds_read_u16 v108, v212 offset:416
	ds_read_u16 v109, v212 offset:432
	ds_read_u16 v110, v212 offset:448
	ds_read_u16 v111, v212 offset:464
	ds_read_u16 v112, v212 offset:480
	ds_read_u16 v113, v212 offset:496
	v_ashrrev_i32_e32 v36, 1, v210
	v_cmp_gt_i32_e32 vcc, 4, v36
	v_add_u32_e32 v37, 12, v117
	v_mov_b32_e32 v54, s9
	v_cndmask_b32_e32 v37, v37, v117, vcc
	v_add_u32_e32 v36, v37, v36
	v_and_b32_e32 v37, 15, v36
	v_mad_u32_u24 v37, v37, s24, v54
	v_lshrrev_b32_e32 v36, 4, v36
	v_lshlrev_b32_e32 v54, 3, v210
	v_mul_lo_u32 v36, v36, s8
	v_and_b32_e32 v54, 8, v54
	v_add3_u32 v36, v37, v36, v54
	v_lshrrev_b32_e32 v37, 2, v214
	s_movk_i32 s8, 0xa40
	v_mul_lo_u32 v37, v37, s8
	v_add_u32_e32 v37, s9, v37
	v_and_b32_e32 v54, 48, v116
	v_mul_lo_u32 v55, v213, s24
	v_add3_u32 v37, v37, v54, v55
	s_waitcnt lgkmcnt(0)
	v_lshlrev_b32_e32 v140, 7, v86
	v_lshl_add_u64 v[244:245], v[114:115], 0, v[140:141]
	global_load_dwordx4 v[38:41], v[244:245], off
	v_lshlrev_b32_e32 v140, 7, v87
	v_lshl_add_u64 v[246:247], v[114:115], 0, v[140:141]
	global_load_dwordx4 v[42:45], v[246:247], off
	v_lshlrev_b32_e32 v140, 7, v88
	v_lshl_add_u64 v[248:249], v[114:115], 0, v[140:141]
	global_load_dwordx4 v[46:49], v[248:249], off
	v_lshlrev_b32_e32 v140, 7, v89
	v_lshl_add_u64 v[250:251], v[114:115], 0, v[140:141]
	global_load_dwordx4 v[50:53], v[250:251], off
	v_lshlrev_b32_e32 v140, 7, v90
	v_lshl_add_u64 v[244:245], v[114:115], 0, v[140:141]
	global_load_dwordx4 v[156:159], v[244:245], off
	v_lshlrev_b32_e32 v140, 7, v91
	v_lshl_add_u64 v[246:247], v[114:115], 0, v[140:141]
	global_load_dwordx4 v[160:163], v[246:247], off
	v_lshlrev_b32_e32 v140, 7, v92
	v_lshl_add_u64 v[248:249], v[114:115], 0, v[140:141]
	global_load_dwordx4 v[164:167], v[248:249], off
	v_lshlrev_b32_e32 v140, 7, v93
	v_lshl_add_u64 v[250:251], v[114:115], 0, v[140:141]
	global_load_dwordx4 v[168:171], v[250:251], off
	v_lshlrev_b32_e32 v140, 7, v94
	v_lshl_add_u64 v[244:245], v[114:115], 0, v[140:141]
	global_load_dwordx4 v[172:175], v[244:245], off
	v_lshlrev_b32_e32 v140, 7, v95
	v_lshl_add_u64 v[246:247], v[114:115], 0, v[140:141]
	global_load_dwordx4 v[176:179], v[246:247], off
	v_lshlrev_b32_e32 v140, 7, v96
	v_lshl_add_u64 v[248:249], v[114:115], 0, v[140:141]
	global_load_dwordx4 v[180:183], v[248:249], off
	v_lshlrev_b32_e32 v140, 7, v97
	v_lshl_add_u64 v[250:251], v[114:115], 0, v[140:141]
	global_load_dwordx4 v[184:187], v[250:251], off
	v_lshlrev_b32_e32 v140, 7, v98
	v_lshl_add_u64 v[244:245], v[114:115], 0, v[140:141]
	global_load_dwordx4 v[188:191], v[244:245], off
	v_lshlrev_b32_e32 v140, 7, v99
	v_lshl_add_u64 v[246:247], v[114:115], 0, v[140:141]
	global_load_dwordx4 v[192:195], v[246:247], off
	v_lshlrev_b32_e32 v140, 7, v100
	v_lshl_add_u64 v[248:249], v[114:115], 0, v[140:141]
	global_load_dwordx4 v[196:199], v[248:249], off
	v_lshlrev_b32_e32 v140, 7, v101
	v_lshl_add_u64 v[250:251], v[114:115], 0, v[140:141]
	global_load_dwordx4 v[224:227], v[250:251], off
	v_lshlrev_b32_e32 v140, 7, v102
	v_lshl_add_u64 v[244:245], v[114:115], 0, v[140:141]
	global_load_dwordx4 v[228:231], v[244:245], off
	v_lshlrev_b32_e32 v140, 7, v103
	v_lshl_add_u64 v[246:247], v[114:115], 0, v[140:141]
	global_load_dwordx4 v[232:235], v[246:247], off
	v_lshlrev_b32_e32 v140, 7, v104
	v_lshl_add_u64 v[248:249], v[114:115], 0, v[140:141]
	global_load_dwordx4 v[236:239], v[248:249], off
	v_lshlrev_b32_e32 v140, 7, v105
	v_lshl_add_u64 v[250:251], v[114:115], 0, v[140:141]
	global_load_dwordx4 v[240:243], v[250:251], off
	s_waitcnt vmcnt(23)
	ds_write_b128 v37, v[2:5]
	s_waitcnt vmcnt(22)
	ds_write_b128 v37, v[6:9] offset:640
	s_waitcnt vmcnt(21)
	ds_write_b128 v37, v[10:13] offset:1312
	s_waitcnt vmcnt(20)
	ds_write_b128 v37, v[14:17] offset:1952
	v_lshlrev_b32_e32 v140, 7, v106
	v_lshl_add_u64 v[244:245], v[114:115], 0, v[140:141]
	global_load_dwordx4 v[2:5], v[244:245], off
	v_lshlrev_b32_e32 v140, 7, v107
	v_lshl_add_u64 v[246:247], v[114:115], 0, v[140:141]
	global_load_dwordx4 v[6:9], v[246:247], off
	v_lshlrev_b32_e32 v140, 7, v108
	v_lshl_add_u64 v[248:249], v[114:115], 0, v[140:141]
	global_load_dwordx4 v[10:13], v[248:249], off
	v_lshlrev_b32_e32 v140, 7, v109
	v_lshl_add_u64 v[250:251], v[114:115], 0, v[140:141]
	global_load_dwordx4 v[14:17], v[250:251], off
	s_waitcnt lgkmcnt(0)
	ds_read_b64_tr_b8 v[86:87], v36 offset:0
	ds_read_b64_tr_b8 v[88:89], v36 offset:16
	ds_read_b64_tr_b8 v[90:91], v36 offset:32
	ds_read_b64_tr_b8 v[92:93], v36 offset:48
	ds_read_b64_tr_b8 v[94:95], v36 offset:2624
	ds_read_b64_tr_b8 v[96:97], v36 offset:2640
	ds_read_b64_tr_b8 v[98:99], v36 offset:2656
	ds_read_b64_tr_b8 v[100:101], v36 offset:2672
	s_waitcnt lgkmcnt(0)
	s_waitcnt vmcnt(23)
	ds_write_b128 v37, v[38:41]
	s_waitcnt vmcnt(22)
	ds_write_b128 v37, v[42:45] offset:640
	s_waitcnt vmcnt(21)
	ds_write_b128 v37, v[46:49] offset:1312
	s_waitcnt vmcnt(20)
	ds_write_b128 v37, v[50:53] offset:1952
	v_lshlrev_b32_e32 v140, 7, v110
	v_lshl_add_u64 v[244:245], v[114:115], 0, v[140:141]
	global_load_dwordx4 v[38:41], v[244:245], off
	v_lshlrev_b32_e32 v140, 7, v111
	v_lshl_add_u64 v[246:247], v[114:115], 0, v[140:141]
	global_load_dwordx4 v[42:45], v[246:247], off
	v_lshlrev_b32_e32 v140, 7, v112
	v_lshl_add_u64 v[248:249], v[114:115], 0, v[140:141]
	global_load_dwordx4 v[46:49], v[248:249], off
	v_lshlrev_b32_e32 v140, 7, v113
	v_lshl_add_u64 v[250:251], v[114:115], 0, v[140:141]
	global_load_dwordx4 v[50:53], v[250:251], off
	v_mfma_f32_16x16x32_fp8_fp8 v[54:57], v[32:33], v[86:87], 0
	v_mfma_f32_16x16x32_fp8_fp8 v[58:61], v[32:33], v[88:89], 0
	v_mfma_f32_16x16x32_fp8_fp8 v[62:65], v[32:33], v[90:91], 0
	v_mfma_f32_16x16x32_fp8_fp8 v[66:69], v[32:33], v[92:93], 0
	v_mfma_f32_16x16x32_fp8_fp8 v[70:73], v[32:33], v[94:95], 0
	v_mfma_f32_16x16x32_fp8_fp8 v[74:77], v[32:33], v[96:97], 0
	v_mfma_f32_16x16x32_fp8_fp8 v[78:81], v[32:33], v[98:99], 0
	v_mfma_f32_16x16x32_fp8_fp8 v[82:85], v[32:33], v[100:101], 0
	s_waitcnt lgkmcnt(0)
	ds_read_b64_tr_b8 v[86:87], v36 offset:0
	ds_read_b64_tr_b8 v[88:89], v36 offset:16
	ds_read_b64_tr_b8 v[90:91], v36 offset:32
	ds_read_b64_tr_b8 v[92:93], v36 offset:48
	ds_read_b64_tr_b8 v[94:95], v36 offset:2624
	ds_read_b64_tr_b8 v[96:97], v36 offset:2640
	ds_read_b64_tr_b8 v[98:99], v36 offset:2656
	ds_read_b64_tr_b8 v[100:101], v36 offset:2672
	s_waitcnt lgkmcnt(0)
	s_waitcnt vmcnt(23)
	ds_write_b128 v37, v[156:159]
	s_waitcnt vmcnt(22)
	ds_write_b128 v37, v[160:163] offset:640
	s_waitcnt vmcnt(21)
	ds_write_b128 v37, v[164:167] offset:1312
	s_waitcnt vmcnt(20)
	ds_write_b128 v37, v[168:171] offset:1952
	v_mfma_f32_16x16x32_fp8_fp8 v[54:57], v[30:31], v[86:87], v[54:57]
	v_mfma_f32_16x16x32_fp8_fp8 v[58:61], v[30:31], v[88:89], v[58:61]
	v_mfma_f32_16x16x32_fp8_fp8 v[62:65], v[30:31], v[90:91], v[62:65]
	v_mfma_f32_16x16x32_fp8_fp8 v[66:69], v[30:31], v[92:93], v[66:69]
	v_mfma_f32_16x16x32_fp8_fp8 v[70:73], v[30:31], v[94:95], v[70:73]
	v_mfma_f32_16x16x32_fp8_fp8 v[74:77], v[30:31], v[96:97], v[74:77]
	v_mfma_f32_16x16x32_fp8_fp8 v[78:81], v[30:31], v[98:99], v[78:81]
	v_mfma_f32_16x16x32_fp8_fp8 v[82:85], v[30:31], v[100:101], v[82:85]
	s_waitcnt lgkmcnt(0)
	ds_read_b64_tr_b8 v[86:87], v36 offset:0
	ds_read_b64_tr_b8 v[88:89], v36 offset:16
	ds_read_b64_tr_b8 v[90:91], v36 offset:32
	ds_read_b64_tr_b8 v[92:93], v36 offset:48
	ds_read_b64_tr_b8 v[94:95], v36 offset:2624
	ds_read_b64_tr_b8 v[96:97], v36 offset:2640
	ds_read_b64_tr_b8 v[98:99], v36 offset:2656
	ds_read_b64_tr_b8 v[100:101], v36 offset:2672
	s_waitcnt lgkmcnt(0)
	s_waitcnt vmcnt(19)
	ds_write_b128 v37, v[172:175]
	s_waitcnt vmcnt(18)
	ds_write_b128 v37, v[176:179] offset:640
	s_waitcnt vmcnt(17)
	ds_write_b128 v37, v[180:183] offset:1312
	s_waitcnt vmcnt(16)
	ds_write_b128 v37, v[184:187] offset:1952
	v_mfma_f32_16x16x32_fp8_fp8 v[54:57], v[28:29], v[86:87], v[54:57]
	v_mfma_f32_16x16x32_fp8_fp8 v[58:61], v[28:29], v[88:89], v[58:61]
	v_mfma_f32_16x16x32_fp8_fp8 v[62:65], v[28:29], v[90:91], v[62:65]
	v_mfma_f32_16x16x32_fp8_fp8 v[66:69], v[28:29], v[92:93], v[66:69]
	v_mfma_f32_16x16x32_fp8_fp8 v[70:73], v[28:29], v[94:95], v[70:73]
	v_mfma_f32_16x16x32_fp8_fp8 v[74:77], v[28:29], v[96:97], v[74:77]
	v_mfma_f32_16x16x32_fp8_fp8 v[78:81], v[28:29], v[98:99], v[78:81]
	v_mfma_f32_16x16x32_fp8_fp8 v[82:85], v[28:29], v[100:101], v[82:85]
	s_waitcnt lgkmcnt(0)
	ds_read_b64_tr_b8 v[86:87], v36 offset:0
	ds_read_b64_tr_b8 v[88:89], v36 offset:16
	ds_read_b64_tr_b8 v[90:91], v36 offset:32
	ds_read_b64_tr_b8 v[92:93], v36 offset:48
	ds_read_b64_tr_b8 v[94:95], v36 offset:2624
	ds_read_b64_tr_b8 v[96:97], v36 offset:2640
	ds_read_b64_tr_b8 v[98:99], v36 offset:2656
	ds_read_b64_tr_b8 v[100:101], v36 offset:2672
	s_waitcnt lgkmcnt(0)
	s_waitcnt vmcnt(15)
	ds_write_b128 v37, v[188:191]
	s_waitcnt vmcnt(14)
	ds_write_b128 v37, v[192:195] offset:640
	s_waitcnt vmcnt(13)
	ds_write_b128 v37, v[196:199] offset:1312
	s_waitcnt vmcnt(12)
	ds_write_b128 v37, v[224:227] offset:1952
	v_mfma_f32_16x16x32_fp8_fp8 v[54:57], v[24:25], v[86:87], v[54:57]
	v_mfma_f32_16x16x32_fp8_fp8 v[58:61], v[24:25], v[88:89], v[58:61]
	v_mfma_f32_16x16x32_fp8_fp8 v[62:65], v[24:25], v[90:91], v[62:65]
	v_mfma_f32_16x16x32_fp8_fp8 v[66:69], v[24:25], v[92:93], v[66:69]
	v_mfma_f32_16x16x32_fp8_fp8 v[70:73], v[24:25], v[94:95], v[70:73]
	v_mfma_f32_16x16x32_fp8_fp8 v[74:77], v[24:25], v[96:97], v[74:77]
	v_mfma_f32_16x16x32_fp8_fp8 v[78:81], v[24:25], v[98:99], v[78:81]
	v_mfma_f32_16x16x32_fp8_fp8 v[82:85], v[24:25], v[100:101], v[82:85]
	s_waitcnt lgkmcnt(0)
	ds_read_b64_tr_b8 v[86:87], v36 offset:0
	ds_read_b64_tr_b8 v[88:89], v36 offset:16
	ds_read_b64_tr_b8 v[90:91], v36 offset:32
	ds_read_b64_tr_b8 v[92:93], v36 offset:48
	ds_read_b64_tr_b8 v[94:95], v36 offset:2624
	ds_read_b64_tr_b8 v[96:97], v36 offset:2640
	ds_read_b64_tr_b8 v[98:99], v36 offset:2656
	ds_read_b64_tr_b8 v[100:101], v36 offset:2672
	s_waitcnt lgkmcnt(0)
	s_waitcnt vmcnt(11)
	ds_write_b128 v37, v[228:231]
	s_waitcnt vmcnt(10)
	ds_write_b128 v37, v[232:235] offset:640
	s_waitcnt vmcnt(9)
	ds_write_b128 v37, v[236:239] offset:1312
	s_waitcnt vmcnt(8)
	ds_write_b128 v37, v[240:243] offset:1952
	v_mfma_f32_16x16x32_fp8_fp8 v[54:57], v[22:23], v[86:87], v[54:57]
	v_mfma_f32_16x16x32_fp8_fp8 v[58:61], v[22:23], v[88:89], v[58:61]
	v_mfma_f32_16x16x32_fp8_fp8 v[62:65], v[22:23], v[90:91], v[62:65]
	v_mfma_f32_16x16x32_fp8_fp8 v[66:69], v[22:23], v[92:93], v[66:69]
	v_mfma_f32_16x16x32_fp8_fp8 v[70:73], v[22:23], v[94:95], v[70:73]
	v_mfma_f32_16x16x32_fp8_fp8 v[74:77], v[22:23], v[96:97], v[74:77]
	v_mfma_f32_16x16x32_fp8_fp8 v[78:81], v[22:23], v[98:99], v[78:81]
	v_mfma_f32_16x16x32_fp8_fp8 v[82:85], v[22:23], v[100:101], v[82:85]
	s_waitcnt lgkmcnt(0)
	ds_read_b64_tr_b8 v[86:87], v36 offset:0
	ds_read_b64_tr_b8 v[88:89], v36 offset:16
	ds_read_b64_tr_b8 v[90:91], v36 offset:32
	ds_read_b64_tr_b8 v[92:93], v36 offset:48
	ds_read_b64_tr_b8 v[94:95], v36 offset:2624
	ds_read_b64_tr_b8 v[96:97], v36 offset:2640
	ds_read_b64_tr_b8 v[98:99], v36 offset:2656
	ds_read_b64_tr_b8 v[100:101], v36 offset:2672
	s_waitcnt lgkmcnt(0)
	s_waitcnt vmcnt(7)
	ds_write_b128 v37, v[2:5]
	s_waitcnt vmcnt(6)
	ds_write_b128 v37, v[6:9] offset:640
	s_waitcnt vmcnt(5)
	ds_write_b128 v37, v[10:13] offset:1312
	s_waitcnt vmcnt(4)
	ds_write_b128 v37, v[14:17] offset:1952
	v_mfma_f32_16x16x32_fp8_fp8 v[54:57], v[20:21], v[86:87], v[54:57]
	v_mfma_f32_16x16x32_fp8_fp8 v[58:61], v[20:21], v[88:89], v[58:61]
	v_mfma_f32_16x16x32_fp8_fp8 v[62:65], v[20:21], v[90:91], v[62:65]
	v_mfma_f32_16x16x32_fp8_fp8 v[66:69], v[20:21], v[92:93], v[66:69]
	v_mfma_f32_16x16x32_fp8_fp8 v[70:73], v[20:21], v[94:95], v[70:73]
	v_mfma_f32_16x16x32_fp8_fp8 v[74:77], v[20:21], v[96:97], v[74:77]
	v_mfma_f32_16x16x32_fp8_fp8 v[78:81], v[20:21], v[98:99], v[78:81]
	v_mfma_f32_16x16x32_fp8_fp8 v[82:85], v[20:21], v[100:101], v[82:85]
	s_waitcnt lgkmcnt(0)
	ds_read_b64_tr_b8 v[86:87], v36 offset:0
	ds_read_b64_tr_b8 v[88:89], v36 offset:16
	ds_read_b64_tr_b8 v[90:91], v36 offset:32
	ds_read_b64_tr_b8 v[92:93], v36 offset:48
	ds_read_b64_tr_b8 v[94:95], v36 offset:2624
	ds_read_b64_tr_b8 v[96:97], v36 offset:2640
	ds_read_b64_tr_b8 v[98:99], v36 offset:2656
	ds_read_b64_tr_b8 v[100:101], v36 offset:2672
	s_waitcnt lgkmcnt(0)
	s_waitcnt vmcnt(3)
	ds_write_b128 v37, v[38:41]
	s_waitcnt vmcnt(2)
	ds_write_b128 v37, v[42:45] offset:640
	s_waitcnt vmcnt(1)
	ds_write_b128 v37, v[46:49] offset:1312
	s_waitcnt vmcnt(0)
	ds_write_b128 v37, v[50:53] offset:1952
	v_mfma_f32_16x16x32_fp8_fp8 v[54:57], v[18:19], v[86:87], v[54:57]
	v_mfma_f32_16x16x32_fp8_fp8 v[58:61], v[18:19], v[88:89], v[58:61]
	v_mfma_f32_16x16x32_fp8_fp8 v[62:65], v[18:19], v[90:91], v[62:65]
	v_mfma_f32_16x16x32_fp8_fp8 v[66:69], v[18:19], v[92:93], v[66:69]
	v_mfma_f32_16x16x32_fp8_fp8 v[70:73], v[18:19], v[94:95], v[70:73]
	v_mfma_f32_16x16x32_fp8_fp8 v[74:77], v[18:19], v[96:97], v[74:77]
	v_mfma_f32_16x16x32_fp8_fp8 v[78:81], v[18:19], v[98:99], v[78:81]
	v_mfma_f32_16x16x32_fp8_fp8 v[82:85], v[18:19], v[100:101], v[82:85]
	s_waitcnt lgkmcnt(0)
	ds_read_b64_tr_b8 v[86:87], v36 offset:0
	ds_read_b64_tr_b8 v[88:89], v36 offset:16
	ds_read_b64_tr_b8 v[90:91], v36 offset:32
	ds_read_b64_tr_b8 v[92:93], v36 offset:48
	ds_read_b64_tr_b8 v[94:95], v36 offset:2624
	ds_read_b64_tr_b8 v[96:97], v36 offset:2640
	ds_read_b64_tr_b8 v[98:99], v36 offset:2656
	ds_read_b64_tr_b8 v[100:101], v36 offset:2672
	s_waitcnt lgkmcnt(0)
	v_mfma_f32_16x16x32_fp8_fp8 v[2:5], v[26:27], v[86:87], v[54:57]
	v_mfma_f32_16x16x32_fp8_fp8 v[6:9], v[26:27], v[88:89], v[58:61]
	v_mfma_f32_16x16x32_fp8_fp8 v[10:13], v[26:27], v[90:91], v[62:65]
	v_mfma_f32_16x16x32_fp8_fp8 v[14:17], v[26:27], v[92:93], v[66:69]
	v_mfma_f32_16x16x32_fp8_fp8 v[18:21], v[26:27], v[94:95], v[70:73]
	v_mfma_f32_16x16x32_fp8_fp8 v[22:25], v[26:27], v[96:97], v[74:77]
	v_mfma_f32_16x16x32_fp8_fp8 v[30:33], v[26:27], v[98:99], v[78:81]
	v_mfma_f32_16x16x32_fp8_fp8 v[26:29], v[26:27], v[100:101], v[82:85]
	v_div_scale_f32 v36, s[8:9], v35, v35, 1.0
	v_rcp_f32_e32 v37, v36
	v_readlane_b32 s8, v254, 62
	s_add_u32 s0, s8, s0
	v_readlane_b32 s8, v254, 63
	s_addc_u32 s1, s8, s1
	v_cmp_gt_i32_e64 s[8:9], 2, v211
	v_fma_f32 v38, -v36, v37, 1.0
	v_fmac_f32_e32 v37, v38, v37
	v_div_scale_f32 v38, vcc, 1.0, v35, 1.0
	v_mul_f32_e32 v39, v38, v37
	v_fma_f32 v40, -v36, v39, v38
	v_fmac_f32_e32 v39, v40, v37
	v_fma_f32 v36, -v36, v39, v38
	v_div_fmas_f32 v36, v36, v37, v39
	v_div_fixup_f32 v35, v36, v35, 1.0
	ds_bpermute_b32 v36, v34, v35
	ds_bpermute_b32 v37, v34, v35 offset:16
	v_cmp_eq_u32_e32 vcc, 0, v211
	s_and_saveexec_b64 s[10:11], s[8:9]
	s_cbranch_execz .LBB0_1336
	v_lshl_add_u32 v38, v211, 8, v210
	v_cndmask_b32_e32 v2, v18, v2, vcc
	s_waitcnt lgkmcnt(0)
	v_cndmask_b32_e32 v18, v37, v36, vcc
	v_mul_f32_e32 v2, v2, v18
	v_ashrrev_i32_e32 v39, 31, v38
	v_cvt_pk_bf16_f32 v2, v2, s0
	v_lshl_add_u64 v[36:37], v[38:39], 1, s[0:1]
	global_store_short v[36:37], v2, off
	v_cndmask_b32_e32 v2, v22, v6, vcc
	v_mul_f32_e32 v2, v2, v18
	v_cvt_pk_bf16_f32 v2, v2, s0
	global_store_short v[36:37], v2, off offset:32
	v_cndmask_b32_e32 v2, v30, v10, vcc
	v_mul_f32_e32 v2, v2, v18
	v_cvt_pk_bf16_f32 v2, v2, s0
	global_store_short v[36:37], v2, off offset:64
	v_cndmask_b32_e32 v2, v26, v14, vcc
	v_mul_f32_e32 v2, v2, v18
	v_cvt_pk_bf16_f32 v2, v2, s0
	global_store_short v[36:37], v2, off offset:96
